# speedup vs baseline: 1.1546x; 1.1546x over previous
_Z8k_layer2PKhPKfPK15HIP_vector_typeIjLj4EEPKjS2_PKDF16_S2_Pf:
	s_lshl_b32 s3, s2, 2
	s_and_b32 s3, s3, 28
	s_and_b32 s12, s2, 0xffffffe0
	s_or_b32 s3, s3, s12
	s_bfe_u32 s12, s2, 0x20003
	s_or_b32 s3, s3, s12
	s_load_dwordx8 s[4:11], s[0:1], 0x0
	s_cmpk_eq_i32 s2, 0x3ef
	s_movk_i32 s12, 0x3f7
	s_cselect_b32 s12, s12, 0x3fb
	s_cmpk_gt_i32 s3, 0x3fc
	s_cselect_b32 s12, s12, s3
	v_lshrrev_b32_e32 v80, 3, v0
	v_lshl_or_b32 v6, s12, 5, v80
	v_ashrrev_i32_e32 v7, 31, v6
	v_or_b32_e32 v83, 0x200, v0
	v_or_b32_e32 v82, 0x300, v0
	s_waitcnt lgkmcnt(0)
	v_lshl_add_u64 v[2:3], v[6:7], 4, s[8:9]
	v_lshlrev_b32_e32 v14, 2, v0
	v_or_b32_e32 v84, 0x100, v0
	v_lshlrev_b32_e32 v7, 2, v83
	v_min_u32_e32 v8, 0x3fc, v82
	global_load_dwordx4 v[2:5], v[2:3], off
	v_lshlrev_b32_e32 v1, 2, v84
	v_lshlrev_b32_e32 v8, 2, v8
	global_load_dword v15, v14, s[6:7]
	global_load_dword v16, v1, s[6:7]
	global_load_dword v17, v7, s[6:7]
	global_load_dword v18, v8, s[6:7]
	s_movk_i32 s13, 0x188
	v_mad_u64_u32 v[6:7], s[8:9], s12, 17, v[6:7]
	v_min_i32_e32 v1, 0xc350, v6
	v_mov_b32_e32 v10, 0xc350
	v_cmp_gt_u32_e32 vcc, s13, v0
	v_lshlrev_b32_e32 v81, 4, v0
	v_and_b32_e32 v60, 0x70, v81
	v_cndmask_b32_e32 v6, v10, v1, vcc
	v_mov_b32_e32 v61, 0
	v_ashrrev_i32_e32 v7, 31, v6
	s_mul_i32 s3, s12, 49
	v_lshl_add_u64 v[8:9], s[4:5], 0, v[60:61]
	v_lshlrev_b64 v[6:7], 7, v[6:7]
	v_lshrrev_b32_e32 v1, 3, v84
	v_lshl_add_u64 v[38:39], v[8:9], 0, v[6:7]
	s_movk_i32 s8, 0x88
	v_add_u32_e32 v6, s3, v1
	v_min_i32_e32 v6, 0xc350, v6
	v_cmp_gt_u32_e32 vcc, s8, v0
	s_ashr_i32 s13, s12, 31
	s_lshl_b64 s[8:9], s[12:13], 2
	v_cndmask_b32_e32 v6, v10, v6, vcc
	v_ashrrev_i32_e32 v7, 31, v6
	v_lshlrev_b64 v[6:7], 7, v[6:7]
	v_lshl_add_u64 v[40:41], v[8:9], 0, v[6:7]
	global_load_dwordx4 v[10:13], v[38:39], off
	global_load_dwordx4 v[6:9], v[40:41], off
	s_add_u32 s8, s6, s8
	s_addc_u32 s9, s7, s9
	s_load_dword s18, s[8:9], 0x0
	s_load_dwordx4 s[12:15], s[0:1], 0x28
	s_load_dwordx2 s[6:7], s[0:1], 0x38
	v_cmp_gt_u32_e32 vcc, 64, v0
	s_waitcnt vmcnt(4)
	s_mov_b32 s40, 0xc030c01
	s_mov_b32 s41, 0xff00ff
	v_mul_f32_e32 v15, 0x4b800000, v15
	v_mul_f32_e32 v16, 0x4b800000, v16
	ds_write2st64_b32 v14, v15, v16 offset0:136 offset1:140
	v_and_b32_e32 v105, 7, v0
	v_sub_co_u32_e64 v106, s[22:23], v105, v3
	v_add_u32_e32 v107, v2, v105
	v_add_u32_e32 v106, v106, v4
	v_cndmask_b32_e64 v106, v106, v107, s[22:23]
	v_mov_b32_e32 v107, 0
	v_lshl_add_u64 v[106:107], v[106:107], 2, s[10:11]
	global_load_dword v104, v[106:107], off
	s_waitcnt vmcnt(3)
	v_mul_f32_e32 v17, 0x4b800000, v17
	v_mul_f32_e32 v18, 0x4b800000, v18
	ds_write2st64_b32 v14, v17, v18 offset0:144 offset1:148
	s_and_saveexec_b64 s[8:9], vcc
	s_cbranch_execz .LBB3_4
	v_cmp_gt_u32_e32 vcc, 49, v0
	v_mov_b32_e32 v15, 1.0
	s_and_saveexec_b64 s[16:17], vcc
	s_cbranch_execz .LBB3_3
	s_load_dwordx2 s[0:1], s[0:1], 0x20
	v_add_u32_e32 v15, s3, v0
	v_min_i32_e32 v16, 0xc34f, v15
	v_ashrrev_i32_e32 v17, 31, v16
	s_waitcnt lgkmcnt(0)
	v_lshl_add_u64 v[16:17], v[16:17], 2, s[0:1]
	global_load_dword v16, v[16:17], off
	s_mov_b32 s0, 0xc350
	v_cmp_gt_i32_e32 vcc, s0, v15
	s_waitcnt vmcnt(0)
	s_nop 0
	v_cndmask_b32_e32 v15, 1.0, v16, vcc

.LBB3_6:
	s_or_b64 exec, exec, s[4:5]
	s_waitcnt vmcnt(4)
	v_and_b32_e32 v113, s41, v14
	v_perm_b32 v114, v14, v14, s40
	v_and_b32_e32 v115, s41, v15
	v_perm_b32 v116, v15, v15, s40
	v_and_b32_e32 v117, s41, v16
	v_perm_b32 v118, v16, v16, s40
	v_cmp_lt_u32_e64 s[0:1], v94, v5
	v_add_u32_e32 v88, -1, v88
	v_and_b32_e32 v119, s41, v17
	v_perm_b32 v120, v17, v17, s40
	v_fma_mix_f32 v68, v117, v48, v68 op_sel:[1,0,0] op_sel_hi:[1,0,0]
	v_fma_mix_f32 v69, v118, v48, v69 op_sel:[1,0,0] op_sel_hi:[1,0,0]
	v_fma_mix_f32 v70, v117, v48, v62 op_sel_hi:[1,0,0]
	v_fma_mix_f32 v71, v118, v48, v63 op_sel_hi:[1,0,0]
	v_cndmask_b32_e64 v14, v51, v97, s[0:1]
	v_cmp_eq_u32_e64 s[0:1], 0, v88
	v_fma_mix_f32 v64, v119, v48, v24 op_sel:[1,0,0] op_sel_hi:[1,0,0]
	v_fma_mix_f32 v65, v120, v48, v25 op_sel:[1,0,0] op_sel_hi:[1,0,0]
	v_fma_mix_f32 v66, v119, v48, v36 op_sel_hi:[1,0,0]
	v_fma_mix_f32 v67, v120, v48, v37 op_sel_hi:[1,0,0]
	v_fma_mix_f32 v72, v115, v48, v22 op_sel:[1,0,0] op_sel_hi:[1,0,0]
	v_fma_mix_f32 v73, v116, v48, v23 op_sel:[1,0,0] op_sel_hi:[1,0,0]
	v_fma_mix_f32 v74, v115, v48, v58 op_sel_hi:[1,0,0]
	v_fma_mix_f32 v75, v116, v48, v59 op_sel_hi:[1,0,0]
	v_fma_mix_f32 v76, v113, v48, v34 op_sel:[1,0,0] op_sel_hi:[1,0,0]
	v_fma_mix_f32 v77, v114, v48, v35 op_sel:[1,0,0] op_sel_hi:[1,0,0]
	v_fma_mix_f32 v78, v113, v48, v28 op_sel_hi:[1,0,0]
	v_fma_mix_f32 v79, v114, v48, v29 op_sel_hi:[1,0,0]
	v_add_u32_e32 v94, 8, v94
	s_or_b64 s[16:17], s[0:1], s[16:17]
	v_mov_b32_e32 v95, v96
	v_mov_b32_e32 v96, v14
	s_andn2_b64 exec, exec, s[16:17]
	s_cbranch_execz .LBB3_23

.LBB3_9:
	s_or_b64 exec, exec, s[4:5]
	s_waitcnt vmcnt(5)
	v_and_b32_e32 v113, s41, v30
	v_perm_b32 v114, v30, v30, s40
	v_fma_mix_f32 v78, v113, v56, v78 op_sel_hi:[1,0,0]
	v_fma_mix_f32 v79, v114, v56, v79 op_sel_hi:[1,0,0]
	v_fma_mix_f32 v76, v113, v56, v76 op_sel:[1,0,0] op_sel_hi:[1,0,0]
	v_fma_mix_f32 v77, v114, v56, v77 op_sel:[1,0,0] op_sel_hi:[1,0,0]
	v_and_b32_e32 v115, s41, v31
	v_perm_b32 v116, v31, v31, s40
	v_fma_mix_f32 v74, v115, v56, v74 op_sel_hi:[1,0,0]
	v_fma_mix_f32 v75, v116, v56, v75 op_sel_hi:[1,0,0]
	v_and_b32_e32 v117, s41, v32
	v_perm_b32 v118, v32, v32, s40
	v_fma_mix_f32 v70, v117, v56, v70 op_sel_hi:[1,0,0]
	v_fma_mix_f32 v71, v118, v56, v71 op_sel_hi:[1,0,0]
	v_fma_mix_f32 v68, v117, v56, v68 op_sel:[1,0,0] op_sel_hi:[1,0,0]
	v_fma_mix_f32 v69, v118, v56, v69 op_sel:[1,0,0] op_sel_hi:[1,0,0]
	v_and_b32_e32 v119, s41, v33
	v_perm_b32 v120, v33, v33, s40
	v_fma_mix_f32 v66, v119, v56, v66 op_sel_hi:[1,0,0]
	v_fma_mix_f32 v67, v120, v56, v67 op_sel_hi:[1,0,0]
	v_and_b32_e32 v32, 2, v52
	v_fma_mix_f32 v72, v115, v56, v72 op_sel:[1,0,0] op_sel_hi:[1,0,0]
	v_fma_mix_f32 v73, v116, v56, v73 op_sel:[1,0,0] op_sel_hi:[1,0,0]
	v_fma_mix_f32 v30, v119, v56, v64 op_sel:[1,0,0] op_sel_hi:[1,0,0]
	v_fma_mix_f32 v31, v120, v56, v65 op_sel:[1,0,0] op_sel_hi:[1,0,0]
	v_cmp_ne_u32_e64 s[0:1], 0, v32
	s_and_saveexec_b64 s[4:5], s[0:1]
	s_cbranch_execz .LBB3_11
	v_and_b32_e32 v32, 63, v98
	v_mul_u32_u24_e32 v32, 0x220, v32
	v_or_b32_e32 v42, v49, v32
	ds_read2_b32 v[32:33], v42 offset1:8
	ds_read2_b32 v[64:65], v42 offset0:16 offset1:24
	ds_read2_b32 v[98:99], v42 offset0:32 offset1:40
	ds_bpermute_b32 v63, v85, v95
	s_waitcnt lgkmcnt(3)
	v_add_f32_e32 v32, v78, v32
	v_add_f32_e32 v33, v79, v33
	s_waitcnt lgkmcnt(2)
	v_add_f32_e32 v53, v76, v64
	ds_write2_b32 v42, v32, v33 offset1:8
	v_add_f32_e32 v32, v77, v65
	ds_write2_b32 v42, v53, v32 offset0:16 offset1:24
	ds_read2_b32 v[32:33], v42 offset0:48 offset1:56
	ds_read2_b32 v[64:65], v42 offset0:64 offset1:72
	s_waitcnt lgkmcnt(5)
	v_add_f32_e32 v53, v74, v98
	v_add_f32_e32 v59, v75, v99
	ds_write2_b32 v42, v53, v59 offset0:32 offset1:40
	s_waitcnt lgkmcnt(2)
	v_add_f32_e32 v32, v72, v32
	v_add_f32_e32 v33, v73, v33
	ds_write2_b32 v42, v32, v33 offset0:48 offset1:56
	ds_read2_b32 v[32:33], v42 offset0:80 offset1:88
	s_waitcnt lgkmcnt(3)
	v_add_f32_e32 v53, v70, v64
	v_add_f32_e32 v59, v71, v65
	ds_read2_b32 v[64:65], v42 offset0:96 offset1:104
	ds_write2_b32 v42, v53, v59 offset0:64 offset1:72
	s_waitcnt lgkmcnt(2)
	v_add_f32_e32 v32, v68, v32
	v_add_f32_e32 v33, v69, v33
	ds_write2_b32 v42, v32, v33 offset0:80 offset1:88
	ds_read2_b32 v[32:33], v42 offset0:112 offset1:120
	s_waitcnt lgkmcnt(3)
	v_add_f32_e32 v53, v66, v64
	v_add_f32_e32 v59, v67, v65
	v_lshrrev_b32_e32 v98, 16, v63
	ds_write2_b32 v42, v53, v59 offset0:96 offset1:104
	s_waitcnt lgkmcnt(1)
	v_add_f32_e32 v30, v30, v32
	v_add_f32_e32 v31, v31, v33
	ds_write2_b32 v42, v30, v31 offset0:112 offset1:120
	v_mov_b32_e32 v30, 0
	v_mov_b32_e32 v31, v30
	v_mov_b32_e32 v66, v30
	v_mov_b32_e32 v67, v30
	v_mov_b32_e32 v68, v30
	v_mov_b32_e32 v69, v30
	v_mov_b32_e32 v70, v30
	v_mov_b32_e32 v71, v30
	v_mov_b32_e32 v72, v30
	v_mov_b32_e32 v73, v30
	v_mov_b32_e32 v74, v30
	v_mov_b32_e32 v75, v30
	v_mov_b32_e32 v76, v30
	v_mov_b32_e32 v77, v30
	v_mov_b32_e32 v78, v30
	v_mov_b32_e32 v79, v30
.LBB3_11:
	s_or_b64 exec, exec, s[4:5]
	v_and_b32_e32 v113, s41, v18
	v_perm_b32 v114, v18, v18, s40
	v_fma_mix_f32 v78, v113, v57, v78 op_sel_hi:[1,0,0]
	v_fma_mix_f32 v79, v114, v57, v79 op_sel_hi:[1,0,0]
	v_fma_mix_f32 v76, v113, v57, v76 op_sel:[1,0,0] op_sel_hi:[1,0,0]
	v_fma_mix_f32 v77, v114, v57, v77 op_sel:[1,0,0] op_sel_hi:[1,0,0]
	v_and_b32_e32 v115, s41, v19
	v_perm_b32 v116, v19, v19, s40
	v_fma_mix_f32 v74, v115, v57, v74 op_sel_hi:[1,0,0]
	v_fma_mix_f32 v75, v116, v57, v75 op_sel_hi:[1,0,0]
	v_and_b32_e32 v117, s41, v20
	v_perm_b32 v118, v20, v20, s40
	v_fma_mix_f32 v70, v117, v57, v70 op_sel_hi:[1,0,0]
	v_fma_mix_f32 v71, v118, v57, v71 op_sel_hi:[1,0,0]
	v_fma_mix_f32 v64, v117, v57, v68 op_sel:[1,0,0] op_sel_hi:[1,0,0]
	v_fma_mix_f32 v65, v118, v57, v69 op_sel:[1,0,0] op_sel_hi:[1,0,0]
	v_and_b32_e32 v119, s41, v21
	v_perm_b32 v120, v21, v21, s40
	v_fma_mix_f32 v72, v115, v57, v72 op_sel:[1,0,0] op_sel_hi:[1,0,0]
	v_fma_mix_f32 v73, v116, v57, v73 op_sel:[1,0,0] op_sel_hi:[1,0,0]
	v_fma_mix_f32 v32, v119, v57, v66 op_sel_hi:[1,0,0]
	v_fma_mix_f32 v33, v120, v57, v67 op_sel_hi:[1,0,0]
	v_and_b32_e32 v20, 4, v52
	v_fma_mix_f32 v18, v119, v57, v30 op_sel:[1,0,0] op_sel_hi:[1,0,0]
	v_fma_mix_f32 v19, v120, v57, v31 op_sel:[1,0,0] op_sel_hi:[1,0,0]
	v_cmp_ne_u32_e64 s[0:1], 0, v20
	s_and_saveexec_b64 s[4:5], s[0:1]
	s_cbranch_execz .LBB3_13
	v_and_b32_e32 v20, 63, v98
	v_mul_u32_u24_e32 v20, 0x220, v20
	v_or_b32_e32 v42, v49, v20
	ds_read2_b32 v[20:21], v42 offset1:8
	ds_read2_b32 v[30:31], v42 offset0:16 offset1:24
	ds_read2_b32 v[56:57], v42 offset0:32 offset1:40
	s_waitcnt lgkmcnt(2)
	v_add_f32_e32 v20, v78, v20
	v_add_f32_e32 v21, v79, v21
	s_waitcnt lgkmcnt(1)
	v_add_f32_e32 v30, v76, v30
	ds_write2_b32 v42, v20, v21 offset1:8
	v_add_f32_e32 v20, v77, v31
	ds_write2_b32 v42, v30, v20 offset0:16 offset1:24
	ds_read2_b32 v[20:21], v42 offset0:48 offset1:56
	s_waitcnt lgkmcnt(3)
	v_add_f32_e32 v30, v74, v56
	v_add_f32_e32 v31, v75, v57
	ds_write2_b32 v42, v30, v31 offset0:32 offset1:40
	ds_read2_b32 v[30:31], v42 offset0:64 offset1:72
	s_waitcnt lgkmcnt(2)
	v_add_f32_e32 v20, v72, v20
	v_add_f32_e32 v21, v73, v21
	ds_write2_b32 v42, v20, v21 offset0:48 offset1:56
	ds_read2_b32 v[20:21], v42 offset0:80 offset1:88
	s_waitcnt lgkmcnt(2)
	v_add_f32_e32 v30, v70, v30
	v_add_f32_e32 v31, v71, v31
	ds_write2_b32 v42, v30, v31 offset0:64 offset1:72
	ds_read2_b32 v[30:31], v42 offset0:96 offset1:104
	s_waitcnt lgkmcnt(2)
	v_add_f32_e32 v20, v64, v20
	v_add_f32_e32 v21, v65, v21
	ds_write2_b32 v42, v20, v21 offset0:80 offset1:88
	ds_read2_b32 v[20:21], v42 offset0:112 offset1:120
	s_waitcnt lgkmcnt(2)
	v_add_f32_e32 v30, v32, v30
	ds_bpermute_b32 v32, v86, v95
	v_add_f32_e32 v31, v33, v31
	ds_write2_b32 v42, v30, v31 offset0:96 offset1:104
	s_waitcnt lgkmcnt(2)
	v_add_f32_e32 v18, v18, v20
	v_add_f32_e32 v19, v19, v21
	ds_write2_b32 v42, v18, v19 offset0:112 offset1:120
	v_mov_b32_e32 v18, 0
	s_waitcnt lgkmcnt(2)
	v_lshrrev_b32_e32 v98, 16, v32
	v_mov_b32_e32 v19, v18
	v_mov_b32_e32 v32, v18
	v_mov_b32_e32 v33, v18
	v_mov_b32_e32 v64, v18
	v_mov_b32_e32 v65, v18
	v_mov_b32_e32 v70, v18
	v_mov_b32_e32 v71, v18
	v_mov_b32_e32 v72, v18
	v_mov_b32_e32 v73, v18
	v_mov_b32_e32 v74, v18
	v_mov_b32_e32 v75, v18
	v_mov_b32_e32 v76, v18
	v_mov_b32_e32 v77, v18
	v_mov_b32_e32 v78, v18
	v_mov_b32_e32 v79, v18
.LBB3_13:
	s_or_b64 exec, exec, s[4:5]
	v_and_b32_e32 v113, s41, v10
	v_perm_b32 v114, v10, v10, s40
	v_fma_mix_f32 v78, v113, v50, v78 op_sel_hi:[1,0,0]
	v_fma_mix_f32 v79, v114, v50, v79 op_sel_hi:[1,0,0]
	v_fma_mix_f32 v76, v113, v50, v76 op_sel:[1,0,0] op_sel_hi:[1,0,0]
	v_fma_mix_f32 v77, v114, v50, v77 op_sel:[1,0,0] op_sel_hi:[1,0,0]
	v_and_b32_e32 v115, s41, v11
	v_perm_b32 v116, v11, v11, s40
	v_fma_mix_f32 v68, v115, v50, v74 op_sel_hi:[1,0,0]
	v_fma_mix_f32 v69, v116, v50, v75 op_sel_hi:[1,0,0]
	v_and_b32_e32 v117, s41, v12
	v_perm_b32 v118, v12, v12, s40
	v_fma_mix_f32 v56, v117, v50, v70 op_sel_hi:[1,0,0]
	v_fma_mix_f32 v57, v118, v50, v71 op_sel_hi:[1,0,0]
	v_fma_mix_f32 v30, v117, v50, v64 op_sel:[1,0,0] op_sel_hi:[1,0,0]
	v_fma_mix_f32 v31, v118, v50, v65 op_sel:[1,0,0] op_sel_hi:[1,0,0]
	v_and_b32_e32 v119, s41, v13
	v_perm_b32 v120, v13, v13, s40
	v_fma_mix_f32 v66, v115, v50, v72 op_sel:[1,0,0] op_sel_hi:[1,0,0]
	v_fma_mix_f32 v67, v116, v50, v73 op_sel:[1,0,0] op_sel_hi:[1,0,0]
	v_fma_mix_f32 v20, v119, v50, v32 op_sel_hi:[1,0,0]
	v_fma_mix_f32 v21, v120, v50, v33 op_sel_hi:[1,0,0]
	v_and_b32_e32 v12, 8, v52
	v_fma_mix_f32 v10, v119, v50, v18 op_sel:[1,0,0] op_sel_hi:[1,0,0]
	v_fma_mix_f32 v11, v120, v50, v19 op_sel:[1,0,0] op_sel_hi:[1,0,0]
	v_cmp_ne_u32_e64 s[0:1], 0, v12
	s_and_saveexec_b64 s[4:5], s[0:1]
	s_cbranch_execz .LBB3_15
	v_and_b32_e32 v12, 63, v98
	v_mul_u32_u24_e32 v12, 0x220, v12
	v_or_b32_e32 v42, v49, v12
	ds_read2_b32 v[12:13], v42 offset1:8
	ds_read2_b32 v[18:19], v42 offset0:16 offset1:24
	ds_read2_b32 v[32:33], v42 offset0:32 offset1:40
	s_waitcnt lgkmcnt(2)
	v_add_f32_e32 v12, v78, v12
	v_add_f32_e32 v13, v79, v13
	s_waitcnt lgkmcnt(1)
	v_add_f32_e32 v18, v76, v18
	ds_write2_b32 v42, v12, v13 offset1:8
	v_add_f32_e32 v12, v77, v19
	ds_write2_b32 v42, v18, v12 offset0:16 offset1:24
	ds_read2_b32 v[12:13], v42 offset0:48 offset1:56
	s_waitcnt lgkmcnt(3)
	v_add_f32_e32 v18, v68, v32
	v_add_f32_e32 v19, v69, v33
	ds_write2_b32 v42, v18, v19 offset0:32 offset1:40
	ds_read2_b32 v[18:19], v42 offset0:64 offset1:72
	s_waitcnt lgkmcnt(2)
	v_add_f32_e32 v12, v66, v12
	v_add_f32_e32 v13, v67, v13
	ds_write2_b32 v42, v12, v13 offset0:48 offset1:56
	ds_read2_b32 v[12:13], v42 offset0:80 offset1:88
	s_waitcnt lgkmcnt(2)
	v_add_f32_e32 v18, v56, v18
	v_add_f32_e32 v19, v57, v19
	ds_write2_b32 v42, v18, v19 offset0:64 offset1:72
	ds_read2_b32 v[18:19], v42 offset0:96 offset1:104
	s_waitcnt lgkmcnt(2)
	v_add_f32_e32 v12, v30, v12
	v_add_f32_e32 v13, v31, v13
	ds_write2_b32 v42, v12, v13 offset0:80 offset1:88
	ds_read2_b32 v[12:13], v42 offset0:112 offset1:120
	s_waitcnt lgkmcnt(2)
	v_add_f32_e32 v18, v20, v18
	ds_bpermute_b32 v20, v87, v95
	v_add_f32_e32 v19, v21, v19
	ds_write2_b32 v42, v18, v19 offset0:96 offset1:104
	s_waitcnt lgkmcnt(2)
	v_add_f32_e32 v10, v10, v12
	v_add_f32_e32 v11, v11, v13
	ds_write2_b32 v42, v10, v11 offset0:112 offset1:120
	v_mov_b32_e32 v10, 0
	s_waitcnt lgkmcnt(2)
	v_lshrrev_b32_e32 v98, 16, v20
	v_mov_b32_e32 v11, v10
	v_mov_b32_e32 v20, v10
	v_mov_b32_e32 v21, v10
	v_mov_b32_e32 v30, v10
	v_mov_b32_e32 v31, v10
	v_mov_b32_e32 v56, v10
	v_mov_b32_e32 v57, v10
	v_mov_b32_e32 v66, v10
	v_mov_b32_e32 v67, v10
	v_mov_b32_e32 v68, v10
	v_mov_b32_e32 v69, v10
	v_mov_b32_e32 v76, v10
	v_mov_b32_e32 v77, v10
	v_mov_b32_e32 v78, v10
	v_mov_b32_e32 v79, v10
.LBB3_15:
	s_or_b64 exec, exec, s[4:5]
	v_and_b32_e32 v113, s41, v6
	v_perm_b32 v114, v6, v6, s40
	v_fma_mix_f32 v78, v113, v46, v78 op_sel_hi:[1,0,0]
	v_fma_mix_f32 v79, v114, v46, v79 op_sel_hi:[1,0,0]
	v_fma_mix_f32 v76, v113, v46, v76 op_sel:[1,0,0] op_sel_hi:[1,0,0]
	v_fma_mix_f32 v77, v114, v46, v77 op_sel:[1,0,0] op_sel_hi:[1,0,0]
	v_and_b32_e32 v115, s41, v7
	v_perm_b32 v116, v7, v7, s40
	v_fma_mix_f32 v74, v115, v46, v68 op_sel_hi:[1,0,0]
	v_fma_mix_f32 v75, v116, v46, v69 op_sel_hi:[1,0,0]
	v_and_b32_e32 v117, s41, v8
	v_perm_b32 v118, v8, v8, s40
	v_fma_mix_f32 v70, v117, v46, v56 op_sel_hi:[1,0,0]
	v_fma_mix_f32 v71, v118, v46, v57 op_sel_hi:[1,0,0]
	v_fma_mix_f32 v68, v117, v46, v30 op_sel:[1,0,0] op_sel_hi:[1,0,0]
	v_fma_mix_f32 v69, v118, v46, v31 op_sel:[1,0,0] op_sel_hi:[1,0,0]
	v_and_b32_e32 v119, s41, v9
	v_perm_b32 v120, v9, v9, s40
	v_fma_mix_f32 v72, v115, v46, v66 op_sel:[1,0,0] op_sel_hi:[1,0,0]
	v_fma_mix_f32 v73, v116, v46, v67 op_sel:[1,0,0] op_sel_hi:[1,0,0]
	v_fma_mix_f32 v66, v119, v46, v20 op_sel_hi:[1,0,0]
	v_fma_mix_f32 v67, v120, v46, v21 op_sel_hi:[1,0,0]
	v_fma_mix_f32 v64, v119, v46, v10 op_sel:[1,0,0] op_sel_hi:[1,0,0]
	v_fma_mix_f32 v65, v120, v46, v11 op_sel:[1,0,0] op_sel_hi:[1,0,0]
	v_sub_u32_e32 v12, v94, v47
	v_add_u32_e32 v12, -12, v12
	v_cmp_lt_u32_e64 s[0:1], v12, v5
	s_cmp_eq_u64 s[0:1], 0
	s_cbranch_scc1 .Lmid_exit_l2
	s_setprio 3
	ds_bpermute_b32 v6, v55, v96
	ds_bpermute_b32 v7, v85, v96
	ds_bpermute_b32 v8, v86, v96
	ds_bpermute_b32 v9, v87, v96
	s_waitcnt lgkmcnt(3)
	v_and_b32_e32 v46, 0xffff, v6
	s_waitcnt lgkmcnt(2)
	v_and_b32_e32 v50, 0xffff, v7
	v_lshlrev_b32_e32 v42, 7, v46
	v_lshl_add_u64 v[6:7], v[44:45], 0, v[42:43]
	v_lshlrev_b32_e32 v42, 7, v50
	s_waitcnt lgkmcnt(1)
	v_and_b32_e32 v53, 0xffff, v8
	global_load_dwordx4 v[30:33], v[6:7], off
	v_lshl_add_u64 v[6:7], v[44:45], 0, v[42:43]
	v_lshlrev_b32_e32 v42, 7, v53
	s_waitcnt lgkmcnt(0)
	v_and_b32_e32 v59, 0xffff, v9
	global_load_dwordx4 v[18:21], v[6:7], off
	v_lshl_add_u64 v[6:7], v[44:45], 0, v[42:43]
	v_lshlrev_b32_e32 v42, 7, v59
	global_load_dwordx4 v[10:13], v[6:7], off
	v_lshl_add_u64 v[6:7], v[44:45], 0, v[42:43]
	global_load_dwordx4 v[6:9], v[6:7], off
	v_mul_hi_u32 v42, v46, s19
	v_lshlrev_b32_e32 v42, 2, v42
	ds_read_b32 v56, v42 offset:34816
	v_mul_hi_u32 v42, v50, s19
	v_lshlrev_b32_e32 v42, 2, v42
	ds_read_b32 v57, v42 offset:34816
	v_mul_hi_u32 v42, v53, s19
	v_lshlrev_b32_e32 v42, 2, v42
	ds_read_b32 v50, v42 offset:34816
	v_mul_hi_u32 v42, v59, s19
	v_lshlrev_b32_e32 v42, 2, v42
	ds_read_b32 v46, v42 offset:34816
	s_setprio 1
	v_and_b32_e32 v42, 16, v52
	v_cmp_ne_u32_e64 s[0:1], 0, v42
	s_and_saveexec_b64 s[4:5], s[0:1]
	s_cbranch_execz .LBB3_17
	v_and_b32_e32 v42, 63, v98
	v_mul_u32_u24_e32 v42, 0x220, v42
	v_or_b32_e32 v42, v49, v42
	ds_read2_b32 v[98:99], v42 offset1:8
	ds_read2_b32 v[100:101], v42 offset0:16 offset1:24
	ds_read2_b32 v[102:103], v42 offset0:32 offset1:40
	s_waitcnt lgkmcnt(2)
	v_add_f32_e32 v53, v78, v98
	v_add_f32_e32 v59, v79, v99
	s_waitcnt lgkmcnt(1)
	v_add_f32_e32 v63, v76, v100
	ds_write2_b32 v42, v53, v59 offset1:8
	v_add_f32_e32 v53, v77, v101
	ds_read2_b32 v[76:77], v42 offset0:48 offset1:56
	ds_write2_b32 v42, v63, v53 offset0:16 offset1:24
	s_waitcnt lgkmcnt(3)
	v_add_f32_e32 v53, v74, v102
	v_add_f32_e32 v59, v75, v103
	ds_read2_b32 v[74:75], v42 offset0:64 offset1:72
	ds_write2_b32 v42, v53, v59 offset0:32 offset1:40
	s_waitcnt lgkmcnt(3)
	v_add_f32_e32 v53, v72, v76
	v_add_f32_e32 v59, v73, v77
	ds_read2_b32 v[72:73], v42 offset0:80 offset1:88
	ds_write2_b32 v42, v53, v59 offset0:48 offset1:56
	s_waitcnt lgkmcnt(3)
	v_add_f32_e32 v53, v70, v74
	v_add_f32_e32 v59, v71, v75
	ds_read2_b32 v[70:71], v42 offset0:96 offset1:104
	ds_write2_b32 v42, v53, v59 offset0:64 offset1:72
	s_waitcnt lgkmcnt(3)
	v_add_f32_e32 v53, v68, v72
	v_add_f32_e32 v59, v69, v73
	ds_read2_b32 v[68:69], v42 offset0:112 offset1:120
	ds_bpermute_b32 v63, v90, v95
	ds_write2_b32 v42, v53, v59 offset0:80 offset1:88
	s_waitcnt lgkmcnt(4)
	v_add_f32_e32 v53, v66, v70
	v_add_f32_e32 v59, v67, v71
	ds_write2_b32 v42, v53, v59 offset0:96 offset1:104
	s_waitcnt lgkmcnt(3)
	v_add_f32_e32 v53, v64, v68
	v_mov_b32_e32 v64, 0
	v_add_f32_e32 v59, v65, v69
	s_waitcnt lgkmcnt(2)
	v_lshrrev_b32_e32 v98, 16, v63
	v_mov_b32_e32 v65, v64
	v_mov_b32_e32 v78, v64
	v_mov_b32_e32 v79, v64
	v_mov_b32_e32 v76, v64
	v_mov_b32_e32 v77, v64
	v_mov_b32_e32 v74, v64
	v_mov_b32_e32 v75, v64
	v_mov_b32_e32 v72, v64
	v_mov_b32_e32 v73, v64
	v_mov_b32_e32 v70, v64
	v_mov_b32_e32 v71, v64
	v_mov_b32_e32 v68, v64
	v_mov_b32_e32 v69, v64
	v_mov_b32_e32 v66, v64
	v_mov_b32_e32 v67, v64
	ds_write2_b32 v42, v53, v59 offset0:112 offset1:120
.LBB3_17:
	s_or_b64 exec, exec, s[4:5]
	s_waitcnt vmcnt(7)
	v_and_b32_e32 v113, s41, v34
	v_perm_b32 v114, v34, v34, s40
	v_fma_mix_f32 v78, v113, v62, v78 op_sel_hi:[1,0,0]
	v_fma_mix_f32 v79, v114, v62, v79 op_sel_hi:[1,0,0]
	v_fma_mix_f32 v76, v113, v62, v76 op_sel:[1,0,0] op_sel_hi:[1,0,0]
	v_fma_mix_f32 v77, v114, v62, v77 op_sel:[1,0,0] op_sel_hi:[1,0,0]
	v_and_b32_e32 v115, s41, v35
	v_perm_b32 v116, v35, v35, s40
	v_fma_mix_f32 v74, v115, v62, v74 op_sel_hi:[1,0,0]
	v_fma_mix_f32 v75, v116, v62, v75 op_sel_hi:[1,0,0]
	v_and_b32_e32 v117, s41, v36
	v_perm_b32 v118, v36, v36, s40
	v_fma_mix_f32 v70, v117, v62, v70 op_sel_hi:[1,0,0]
	v_fma_mix_f32 v71, v118, v62, v71 op_sel_hi:[1,0,0]
	v_fma_mix_f32 v68, v117, v62, v68 op_sel:[1,0,0] op_sel_hi:[1,0,0]
	v_fma_mix_f32 v69, v118, v62, v69 op_sel:[1,0,0] op_sel_hi:[1,0,0]
	v_and_b32_e32 v119, s41, v37
	v_perm_b32 v120, v37, v37, s40
	v_fma_mix_f32 v66, v119, v62, v66 op_sel_hi:[1,0,0]
	v_fma_mix_f32 v67, v120, v62, v67 op_sel_hi:[1,0,0]
	v_and_b32_e32 v36, 32, v52
	v_fma_mix_f32 v72, v115, v62, v72 op_sel:[1,0,0] op_sel_hi:[1,0,0]
	v_fma_mix_f32 v73, v116, v62, v73 op_sel:[1,0,0] op_sel_hi:[1,0,0]
	v_fma_mix_f32 v34, v119, v62, v64 op_sel:[1,0,0] op_sel_hi:[1,0,0]
	v_fma_mix_f32 v35, v120, v62, v65 op_sel:[1,0,0] op_sel_hi:[1,0,0]
	v_cmp_ne_u32_e64 s[0:1], 0, v36
	s_and_saveexec_b64 s[4:5], s[0:1]
	s_cbranch_execz .LBB3_19
	v_and_b32_e32 v36, 63, v98
	v_mul_u32_u24_e32 v36, 0x220, v36
	v_or_b32_e32 v42, v49, v36
	ds_read2_b32 v[36:37], v42 offset1:8
	ds_read2_b32 v[62:63], v42 offset0:16 offset1:24
	ds_read2_b32 v[64:65], v42 offset0:32 offset1:40
	s_waitcnt lgkmcnt(2)
	v_add_f32_e32 v36, v78, v36
	v_add_f32_e32 v37, v79, v37
	s_waitcnt lgkmcnt(1)
	v_add_f32_e32 v53, v76, v62
	ds_write2_b32 v42, v36, v37 offset1:8
	v_add_f32_e32 v36, v77, v63
	ds_write2_b32 v42, v53, v36 offset0:16 offset1:24
	ds_read2_b32 v[36:37], v42 offset0:48 offset1:56
	ds_read2_b32 v[62:63], v42 offset0:64 offset1:72
	s_waitcnt lgkmcnt(4)
	v_add_f32_e32 v53, v74, v64
	v_add_f32_e32 v59, v75, v65
	ds_write2_b32 v42, v53, v59 offset0:32 offset1:40
	s_waitcnt lgkmcnt(2)
	v_add_f32_e32 v36, v72, v36
	v_add_f32_e32 v37, v73, v37
	ds_write2_b32 v42, v36, v37 offset0:48 offset1:56
	ds_read2_b32 v[36:37], v42 offset0:80 offset1:88
	s_waitcnt lgkmcnt(3)
	v_add_f32_e32 v53, v70, v62
	v_add_f32_e32 v59, v71, v63
	ds_read2_b32 v[62:63], v42 offset0:96 offset1:104
	ds_write2_b32 v42, v53, v59 offset0:64 offset1:72
	s_waitcnt lgkmcnt(2)
	v_add_f32_e32 v36, v68, v36
	v_add_f32_e32 v37, v69, v37
	ds_write2_b32 v42, v36, v37 offset0:80 offset1:88
	ds_read2_b32 v[36:37], v42 offset0:112 offset1:120
	s_waitcnt lgkmcnt(3)
	v_add_f32_e32 v53, v66, v62
	ds_bpermute_b32 v62, v91, v95
	v_add_f32_e32 v59, v67, v63
	ds_write2_b32 v42, v53, v59 offset0:96 offset1:104
	s_waitcnt lgkmcnt(2)
	v_add_f32_e32 v34, v34, v36
	v_add_f32_e32 v35, v35, v37
	ds_write2_b32 v42, v34, v35 offset0:112 offset1:120
	v_mov_b32_e32 v34, 0
	s_waitcnt lgkmcnt(2)
	v_lshrrev_b32_e32 v98, 16, v62
	v_mov_b32_e32 v35, v34
	v_mov_b32_e32 v66, v34
	v_mov_b32_e32 v67, v34
	v_mov_b32_e32 v68, v34
	v_mov_b32_e32 v69, v34
	v_mov_b32_e32 v70, v34
	v_mov_b32_e32 v71, v34
	v_mov_b32_e32 v72, v34
	v_mov_b32_e32 v73, v34
	v_mov_b32_e32 v74, v34
	v_mov_b32_e32 v75, v34
	v_mov_b32_e32 v76, v34
	v_mov_b32_e32 v77, v34
	v_mov_b32_e32 v78, v34
	v_mov_b32_e32 v79, v34
.LBB3_19:
	s_or_b64 exec, exec, s[4:5]
	s_waitcnt vmcnt(6)
	v_and_b32_e32 v113, s41, v26
	v_perm_b32 v114, v26, v26, s40
	v_fma_mix_f32 v78, v113, v58, v78 op_sel_hi:[1,0,0]
	v_fma_mix_f32 v79, v114, v58, v79 op_sel_hi:[1,0,0]
	v_fma_mix_f32 v76, v113, v58, v76 op_sel:[1,0,0] op_sel_hi:[1,0,0]
	v_fma_mix_f32 v77, v114, v58, v77 op_sel:[1,0,0] op_sel_hi:[1,0,0]
	v_and_b32_e32 v115, s41, v27
	v_perm_b32 v116, v27, v27, s40
	v_fma_mix_f32 v74, v115, v58, v74 op_sel_hi:[1,0,0]
	v_fma_mix_f32 v75, v116, v58, v75 op_sel_hi:[1,0,0]
	v_and_b32_e32 v117, s41, v28
	v_perm_b32 v118, v28, v28, s40
	v_fma_mix_f32 v62, v117, v58, v70 op_sel_hi:[1,0,0]
	v_fma_mix_f32 v63, v118, v58, v71 op_sel_hi:[1,0,0]
	v_fma_mix_f32 v64, v117, v58, v68 op_sel:[1,0,0] op_sel_hi:[1,0,0]
	v_fma_mix_f32 v65, v118, v58, v69 op_sel:[1,0,0] op_sel_hi:[1,0,0]
	v_and_b32_e32 v119, s41, v29
	v_perm_b32 v120, v29, v29, s40
	v_fma_mix_f32 v72, v115, v58, v72 op_sel:[1,0,0] op_sel_hi:[1,0,0]
	v_fma_mix_f32 v73, v116, v58, v73 op_sel:[1,0,0] op_sel_hi:[1,0,0]
	v_fma_mix_f32 v36, v119, v58, v66 op_sel_hi:[1,0,0]
	v_fma_mix_f32 v37, v120, v58, v67 op_sel_hi:[1,0,0]
	v_and_b32_e32 v28, 64, v52
	v_fma_mix_f32 v26, v119, v58, v34 op_sel:[1,0,0] op_sel_hi:[1,0,0]
	v_fma_mix_f32 v27, v120, v58, v35 op_sel:[1,0,0] op_sel_hi:[1,0,0]
	v_cmp_ne_u32_e64 s[0:1], 0, v28
	s_and_saveexec_b64 s[4:5], s[0:1]
	s_cbranch_execz .LBB3_21
	v_and_b32_e32 v28, 63, v98
	v_mul_u32_u24_e32 v28, 0x220, v28
	v_or_b32_e32 v42, v49, v28
	ds_read2_b32 v[28:29], v42 offset1:8
	ds_read2_b32 v[34:35], v42 offset0:16 offset1:24
	ds_read2_b32 v[58:59], v42 offset0:32 offset1:40
	s_waitcnt lgkmcnt(2)
	v_add_f32_e32 v28, v78, v28
	v_add_f32_e32 v29, v79, v29
	s_waitcnt lgkmcnt(1)
	v_add_f32_e32 v34, v76, v34
	ds_write2_b32 v42, v28, v29 offset1:8
	v_add_f32_e32 v28, v77, v35
	ds_write2_b32 v42, v34, v28 offset0:16 offset1:24
	ds_read2_b32 v[28:29], v42 offset0:48 offset1:56
	s_waitcnt lgkmcnt(3)
	v_add_f32_e32 v34, v74, v58
	v_add_f32_e32 v35, v75, v59
	ds_write2_b32 v42, v34, v35 offset0:32 offset1:40
	ds_read2_b32 v[34:35], v42 offset0:64 offset1:72
	s_waitcnt lgkmcnt(2)
	v_add_f32_e32 v28, v72, v28
	v_add_f32_e32 v29, v73, v29
	ds_write2_b32 v42, v28, v29 offset0:48 offset1:56
	ds_read2_b32 v[28:29], v42 offset0:80 offset1:88
	s_waitcnt lgkmcnt(2)
	v_add_f32_e32 v34, v62, v34
	v_add_f32_e32 v35, v63, v35
	ds_write2_b32 v42, v34, v35 offset0:64 offset1:72
	ds_read2_b32 v[34:35], v42 offset0:96 offset1:104
	s_waitcnt lgkmcnt(2)
	v_add_f32_e32 v28, v64, v28
	v_add_f32_e32 v29, v65, v29
	ds_write2_b32 v42, v28, v29 offset0:80 offset1:88
	ds_read2_b32 v[28:29], v42 offset0:112 offset1:120
	s_waitcnt lgkmcnt(2)
	v_add_f32_e32 v34, v36, v34
	ds_bpermute_b32 v36, v92, v95
	v_add_f32_e32 v35, v37, v35
	ds_write2_b32 v42, v34, v35 offset0:96 offset1:104
	s_waitcnt lgkmcnt(2)
	v_add_f32_e32 v26, v26, v28
	v_add_f32_e32 v27, v27, v29
	ds_write2_b32 v42, v26, v27 offset0:112 offset1:120
	v_mov_b32_e32 v26, 0
	s_waitcnt lgkmcnt(2)
	v_lshrrev_b32_e32 v98, 16, v36
	v_mov_b32_e32 v27, v26
	v_mov_b32_e32 v36, v26
	v_mov_b32_e32 v37, v26
	v_mov_b32_e32 v64, v26
	v_mov_b32_e32 v65, v26
	v_mov_b32_e32 v62, v26
	v_mov_b32_e32 v63, v26
	v_mov_b32_e32 v72, v26
	v_mov_b32_e32 v73, v26
	v_mov_b32_e32 v74, v26
	v_mov_b32_e32 v75, v26
	v_mov_b32_e32 v76, v26
	v_mov_b32_e32 v77, v26
	v_mov_b32_e32 v78, v26
	v_mov_b32_e32 v79, v26
.LBB3_21:
	s_or_b64 exec, exec, s[4:5]
	s_waitcnt vmcnt(5)
	v_and_b32_e32 v113, s41, v23
	v_perm_b32 v114, v23, v23, s40
	v_and_b32_e32 v115, s41, v22
	v_perm_b32 v116, v22, v22, s40
	v_fma_mix_f32 v22, v113, v54, v72 op_sel:[1,0,0] op_sel_hi:[1,0,0]
	v_fma_mix_f32 v23, v114, v54, v73 op_sel:[1,0,0] op_sel_hi:[1,0,0]
	v_and_b32_e32 v117, s41, v24
	v_perm_b32 v118, v24, v24, s40
	v_fma_mix_f32 v62, v117, v54, v62 op_sel_hi:[1,0,0]
	v_fma_mix_f32 v63, v118, v54, v63 op_sel_hi:[1,0,0]
	v_fma_mix_f32 v68, v117, v54, v64 op_sel:[1,0,0] op_sel_hi:[1,0,0]
	v_fma_mix_f32 v69, v118, v54, v65 op_sel:[1,0,0] op_sel_hi:[1,0,0]
	v_and_b32_e32 v119, s41, v25
	v_perm_b32 v120, v25, v25, s40
	v_fma_mix_f32 v36, v119, v54, v36 op_sel_hi:[1,0,0]
	v_fma_mix_f32 v37, v120, v54, v37 op_sel_hi:[1,0,0]
	v_fma_mix_f32 v24, v119, v54, v26 op_sel:[1,0,0] op_sel_hi:[1,0,0]
	v_fma_mix_f32 v25, v120, v54, v27 op_sel:[1,0,0] op_sel_hi:[1,0,0]
	v_and_b32_e32 v26, 0x80, v52
	v_fma_mix_f32 v28, v115, v54, v78 op_sel_hi:[1,0,0]
	v_fma_mix_f32 v29, v116, v54, v79 op_sel_hi:[1,0,0]
	v_fma_mix_f32 v34, v115, v54, v76 op_sel:[1,0,0] op_sel_hi:[1,0,0]
	v_fma_mix_f32 v35, v116, v54, v77 op_sel:[1,0,0] op_sel_hi:[1,0,0]
	v_fma_mix_f32 v58, v113, v54, v74 op_sel_hi:[1,0,0]
	v_fma_mix_f32 v59, v114, v54, v75 op_sel_hi:[1,0,0]
	v_cmp_ne_u32_e64 s[0:1], 0, v26
	s_and_saveexec_b64 s[4:5], s[0:1]
	s_cbranch_execz .LBB3_6
	v_and_b32_e32 v26, 63, v98
	v_mul_u32_u24_e32 v26, 0x220, v26
	v_or_b32_e32 v42, v49, v26
	ds_read2_b32 v[26:27], v42 offset1:8
	ds_read2_b32 v[52:53], v42 offset0:16 offset1:24
	ds_read2_b32 v[64:65], v42 offset0:32 offset1:40
	s_waitcnt lgkmcnt(2)
	v_add_f32_e32 v26, v28, v26
	v_add_f32_e32 v27, v29, v27
	s_waitcnt lgkmcnt(1)
	v_add_f32_e32 v28, v34, v52
	ds_write2_b32 v42, v26, v27 offset1:8
	v_add_f32_e32 v26, v35, v53
	ds_write2_b32 v42, v28, v26 offset0:16 offset1:24
	ds_read2_b32 v[26:27], v42 offset0:48 offset1:56
	s_waitcnt lgkmcnt(3)
	v_add_f32_e32 v28, v58, v64
	v_add_f32_e32 v29, v59, v65
	ds_write2_b32 v42, v28, v29 offset0:32 offset1:40
	ds_read2_b32 v[28:29], v42 offset0:64 offset1:72
	s_waitcnt lgkmcnt(2)
	v_add_f32_e32 v22, v22, v26
	v_add_f32_e32 v23, v23, v27
	ds_write2_b32 v42, v22, v23 offset0:48 offset1:56
	ds_read2_b32 v[22:23], v42 offset0:80 offset1:88
	s_waitcnt lgkmcnt(2)
	v_add_f32_e32 v26, v62, v28
	v_add_f32_e32 v27, v63, v29
	ds_write2_b32 v42, v26, v27 offset0:64 offset1:72
	ds_read2_b32 v[26:27], v42 offset0:96 offset1:104
	s_waitcnt lgkmcnt(2)
	v_add_f32_e32 v22, v68, v22
	v_add_f32_e32 v23, v69, v23
	ds_write2_b32 v42, v22, v23 offset0:80 offset1:88
	ds_read2_b32 v[22:23], v42 offset0:112 offset1:120
	ds_bpermute_b32 v28, v93, v95
	s_waitcnt lgkmcnt(3)
	v_add_f32_e32 v26, v36, v26
	v_add_f32_e32 v27, v37, v27
	ds_write2_b32 v42, v26, v27 offset0:96 offset1:104
	s_waitcnt lgkmcnt(2)
	v_add_f32_e32 v22, v24, v22
	v_add_f32_e32 v23, v25, v23
	v_mov_b32_e32 v24, 0
	ds_write2_b32 v42, v22, v23 offset0:112 offset1:120
	s_waitcnt lgkmcnt(2)
	v_lshrrev_b32_e32 v98, 16, v28
	v_mov_b32_e32 v25, v24
	v_mov_b32_e32 v36, v24
	v_mov_b32_e32 v37, v24
	v_mov_b32_e32 v68, v24
	v_mov_b32_e32 v69, v24
	v_mov_b32_e32 v62, v24
	v_mov_b32_e32 v63, v24
	v_mov_b32_e32 v22, v24
	v_mov_b32_e32 v23, v24
	v_mov_b32_e32 v58, v24
	v_mov_b32_e32 v59, v24
	v_mov_b32_e32 v34, v24
	v_mov_b32_e32 v35, v24
	v_mov_b32_e32 v28, v24
	v_mov_b32_e32 v29, v24
	s_branch .LBB3_6

amdhsa.kernels:
  - .agpr_count:     0
    .args:
      - .actual_access:  read_only
        .address_space:  global
        .offset:         0
        .size:           8
        .value_kind:     global_buffer
      - .actual_access:  read_only
        .address_space:  global
        .offset:         8
        .size:           8
        .value_kind:     global_buffer
      - .actual_access:  write_only
        .address_space:  global
        .offset:         16
        .size:           8
        .value_kind:     global_buffer
      - .actual_access:  write_only
        .address_space:  global
        .offset:         24
        .size:           8
        .value_kind:     global_buffer
      - .actual_access:  read_only
        .address_space:  global
        .offset:         32
        .size:           8
        .value_kind:     global_buffer
      - .actual_access:  read_only
        .address_space:  global
        .offset:         40
        .size:           8
        .value_kind:     global_buffer
      - .actual_access:  read_only
        .address_space:  global
        .offset:         48
        .size:           8
        .value_kind:     global_buffer
      - .actual_access:  read_only
        .address_space:  global
        .offset:         56
        .size:           8
        .value_kind:     global_buffer
      - .actual_access:  read_only
        .address_space:  global
        .offset:         64
        .size:           8
        .value_kind:     global_buffer
      - .actual_access:  write_only
        .address_space:  global
        .offset:         72
        .size:           8
        .value_kind:     global_buffer
      - .actual_access:  write_only
        .address_space:  global
        .offset:         80
        .size:           8
        .value_kind:     global_buffer
      - .actual_access:  write_only
        .address_space:  global
        .offset:         88
        .size:           8
        .value_kind:     global_buffer
      - .actual_access:  write_only
        .address_space:  global
        .offset:         96
        .size:           8
        .value_kind:     global_buffer
      - .actual_access:  write_only
        .address_space:  global
        .offset:         104
        .size:           8
        .value_kind:     global_buffer
      - .actual_access:  write_only
        .address_space:  global
        .offset:         112
        .size:           8
        .value_kind:     global_buffer
      - .offset:         120
        .size:           4
        .value_kind:     hidden_block_count_x
      - .offset:         124
        .size:           4
        .value_kind:     hidden_block_count_y
      - .offset:         128
        .size:           4
        .value_kind:     hidden_block_count_z
      - .offset:         132
        .size:           2
        .value_kind:     hidden_group_size_x
      - .offset:         134
        .size:           2
        .value_kind:     hidden_group_size_y
      - .offset:         136
        .size:           2
        .value_kind:     hidden_group_size_z
      - .offset:         138
        .size:           2
        .value_kind:     hidden_remainder_x
      - .offset:         140
        .size:           2
        .value_kind:     hidden_remainder_y
      - .offset:         142
        .size:           2
        .value_kind:     hidden_remainder_z
      - .offset:         160
        .size:           8
        .value_kind:     hidden_global_offset_x
      - .offset:         168
        .size:           8
        .value_kind:     hidden_global_offset_y
      - .offset:         176
        .size:           8
        .value_kind:     hidden_global_offset_z
      - .offset:         184
        .size:           2
        .value_kind:     hidden_grid_dims
    .group_segment_fixed_size: 21520
    .kernarg_segment_align: 8
    .kernarg_segment_size: 376
    .language:       OpenCL C
    .language_version:
      - 2
      - 0
    .max_flat_workgroup_size: 1024
    .name:           _Z11k_chunksortPKiS0_PjS1_PKfS3_S3_S3_S3_PDF16_S4_PfS5_S4_Ph
    .private_segment_fixed_size: 0
    .sgpr_count:     32
    .sgpr_spill_count: 0
    .symbol:         _Z11k_chunksortPKiS0_PjS1_PKfS3_S3_S3_S3_PDF16_S4_PfS5_S4_Ph.kd
    .uniform_work_group_size: 1
    .uses_dynamic_stack: false
    .vgpr_count:     38
    .vgpr_spill_count: 0
    .wavefront_size: 64
  - .agpr_count:     0
    .args:
      - .actual_access:  read_only
        .address_space:  global
        .offset:         0
        .size:           8
        .value_kind:     global_buffer
      - .actual_access:  read_only
        .address_space:  global
        .offset:         8
        .size:           8
        .value_kind:     global_buffer
      - .actual_access:  read_only
        .address_space:  global
        .offset:         16
        .size:           8
        .value_kind:     global_buffer
      - .actual_access:  write_only
        .address_space:  global
        .offset:         24
        .size:           8
        .value_kind:     global_buffer
      - .actual_access:  write_only
        .address_space:  global
        .offset:         32
        .size:           8
        .value_kind:     global_buffer
      - .actual_access:  write_only
        .address_space:  global
        .offset:         40
        .size:           8
        .value_kind:     global_buffer
      - .actual_access:  write_only
        .address_space:  global
        .offset:         48
        .size:           8
        .value_kind:     global_buffer
    .group_segment_fixed_size: 22536
    .kernarg_segment_align: 8
    .kernarg_segment_size: 56
    .language:       OpenCL C
    .language_version:
      - 2
      - 0
    .max_flat_workgroup_size: 1024
    .name:           _Z5k_csrPKjS0_PKfPjPfPDF16_P15HIP_vector_typeIjLj4EE
    .private_segment_fixed_size: 0
    .sgpr_count:     44
    .sgpr_spill_count: 0
    .symbol:         _Z5k_csrPKjS0_PKfPjPfPDF16_P15HIP_vector_typeIjLj4EE.kd
    .uniform_work_group_size: 1
    .uses_dynamic_stack: false
    .vgpr_count:     48
    .vgpr_spill_count: 0
    .wavefront_size: 64
  - .agpr_count:     0
    .args:
      - .actual_access:  read_only
        .address_space:  global
        .offset:         0
        .size:           8
        .value_kind:     global_buffer
      - .actual_access:  read_only
        .address_space:  global
        .offset:         8
        .size:           8
        .value_kind:     global_buffer
      - .actual_access:  read_only
        .address_space:  global
        .offset:         16
        .size:           8
        .value_kind:     global_buffer
      - .actual_access:  read_only
        .address_space:  global
        .offset:         24
        .size:           8
        .value_kind:     global_buffer
      - .actual_access:  read_only
        .address_space:  global
        .offset:         32
        .size:           8
        .value_kind:     global_buffer
      - .actual_access:  read_only
        .address_space:  global
        .offset:         40
        .size:           8
        .value_kind:     global_buffer
      - .actual_access:  read_only
        .address_space:  global
        .offset:         48
        .size:           8
        .value_kind:     global_buffer
      - .actual_access:  write_only
        .address_space:  global
        .offset:         56
        .size:           8
        .value_kind:     global_buffer
      - .actual_access:  write_only
        .address_space:  global
        .offset:         64
        .size:           8
        .value_kind:     global_buffer
    .group_segment_fixed_size: 36112
    .kernarg_segment_align: 8
    .kernarg_segment_size: 72
    .language:       OpenCL C
    .language_version:
      - 2
      - 0
    .max_flat_workgroup_size: 256
    .name:           _Z8k_layer1PKfPKDF16_PK15HIP_vector_typeIjLj4EEPKjS0_S2_S0_PhPf
    .private_segment_fixed_size: 0
    .sgpr_count:     30
    .sgpr_spill_count: 0
    .symbol:         _Z8k_layer1PKfPKDF16_PK15HIP_vector_typeIjLj4EEPKjS0_S2_S0_PhPf.kd
    .uniform_work_group_size: 1
    .uses_dynamic_stack: false
    .vgpr_count:     128
    .vgpr_spill_count: 0
    .wavefront_size: 64
  - .agpr_count:     0
    .args:
      - .actual_access:  read_only
        .address_space:  global
        .offset:         0
        .size:           8
        .value_kind:     global_buffer
      - .actual_access:  read_only
        .address_space:  global
        .offset:         8
        .size:           8
        .value_kind:     global_buffer
      - .actual_access:  read_only
        .address_space:  global
        .offset:         16
        .size:           8
        .value_kind:     global_buffer
      - .actual_access:  read_only
        .address_space:  global
        .offset:         24
        .size:           8
        .value_kind:     global_buffer
      - .actual_access:  read_only
        .address_space:  global
        .offset:         32
        .size:           8
        .value_kind:     global_buffer
      - .actual_access:  read_only
        .address_space:  global
        .offset:         40
        .size:           8
        .value_kind:     global_buffer
      - .actual_access:  read_only
        .address_space:  global
        .offset:         48
        .size:           8
        .value_kind:     global_buffer
      - .address_space:  global
        .offset:         56
        .size:           8
        .value_kind:     global_buffer
    .group_segment_fixed_size: 39168
    .kernarg_segment_align: 8
    .kernarg_segment_size: 64
    .language:       OpenCL C
    .language_version:
      - 2
      - 0
    .max_flat_workgroup_size: 256
    .name:           _Z8k_layer2PKhPKfPK15HIP_vector_typeIjLj4EEPKjS2_PKDF16_S2_Pf
    .private_segment_fixed_size: 0
    .sgpr_count:     27
    .sgpr_spill_count: 0
    .symbol:         _Z8k_layer2PKhPKfPK15HIP_vector_typeIjLj4EEPKjS2_PKDF16_S2_Pf.kd
    .uniform_work_group_size: 1
    .uses_dynamic_stack: false
    .vgpr_count:     128
    .vgpr_spill_count: 0
    .wavefront_size: 64
  - .agpr_count:     0
    .args:
      - .actual_access:  read_only
        .address_space:  global
        .offset:         0
        .size:           8
        .value_kind:     global_buffer
      - .actual_access:  read_only
        .address_space:  global
        .offset:         8
        .size:           8
        .value_kind:     global_buffer
      - .actual_access:  read_only
        .address_space:  global
        .offset:         16
        .size:           8
        .value_kind:     global_buffer
      - .actual_access:  read_only
        .address_space:  global
        .offset:         24
        .size:           8
        .value_kind:     global_buffer
      - .actual_access:  read_only
        .address_space:  global
        .offset:         32
        .size:           8
        .value_kind:     global_buffer
      - .actual_access:  write_only
        .address_space:  global
        .offset:         40
        .size:           8
        .value_kind:     global_buffer
    .group_segment_fixed_size: 512
    .kernarg_segment_align: 8
    .kernarg_segment_size: 48
    .language:       OpenCL C
    .language_version:
      - 2
      - 0
    .max_flat_workgroup_size: 320
    .name:           _Z7k_headsPKfS0_S0_S0_S0_Pf
    .private_segment_fixed_size: 0
    .sgpr_count:     22
    .sgpr_spill_count: 0
    .symbol:         _Z7k_headsPKfS0_S0_S0_S0_Pf.kd
    .uniform_work_group_size: 1
    .uses_dynamic_stack: false
    .vgpr_count:     56
    .vgpr_spill_count: 0
    .wavefront_size: 64
